# attention first half-step: V^T fragment LDS reads issued one per Q.K chunk as their registers free up, P.V MFMAs wait per fragment (on v27)
# baseline (speedup 1.0000x reference)
.LBB0_1240:
	s_mul_i32 s13, s14, 0x6400
	v_add_u32_e32 v86, s13, v185
	ds_read_b128 v[82:85], v86
	ds_read_b128 v[188:191], v86 offset:32
	ds_read_b128 v[192:195], v86 offset:64
	ds_read_b128 v[196:199], v86 offset:96
	ds_read_b128 v[200:203], v86 offset:128
	ds_read_b128 v[216:219], v86 offset:160
	ds_read_b128 v[220:223], v86 offset:192
	ds_read_b128 v[224:227], v86 offset:224
	ds_read_b128 v[228:231], v86 offset:256
	ds_read_b128 v[232:235], v86 offset:288
	ds_read_b128 v[236:239], v86 offset:320
	ds_read_b128 v[240:243], v86 offset:352
	s_waitcnt lgkmcnt(11)
	v_mfma_f32_32x32x16_bf16 v[82:97], v[82:85], v[142:145], 0
	v_sub_f32_e32 v66, v66, v183
	v_sub_f32_e32 v78, v78, v183
	v_exp_f32_e32 v66, v66
	v_exp_f32_e32 v78, v78
	s_waitcnt lgkmcnt(10)
	v_mfma_f32_32x32x16_bf16 v[82:97], v[188:191], v[138:141], v[82:97]
	v_sub_f32_e32 v67, v67, v183
	v_sub_f32_e32 v79, v79, v183
	v_exp_f32_e32 v67, v67
	v_exp_f32_e32 v79, v79
	v_cvt_pk_bf16_f32 v188, v66, v67
	s_waitcnt lgkmcnt(9)
	v_mfma_f32_32x32x16_bf16 v[82:97], v[192:195], v[134:137], v[82:97]
	v_sub_f32_e32 v68, v68, v183
	v_sub_f32_e32 v80, v80, v183
	v_exp_f32_e32 v68, v68
	v_exp_f32_e32 v80, v80
	s_waitcnt lgkmcnt(8)
	v_mfma_f32_32x32x16_bf16 v[82:97], v[196:199], v[130:133], v[82:97]
	v_add_u32_e32 v204, s12, v187
	v_sub_f32_e32 v69, v69, v183
	v_sub_f32_e32 v81, v81, v183
	v_exp_f32_e32 v69, v69
	v_exp_f32_e32 v81, v81
	v_cvt_pk_bf16_f32 v194, v78, v79
	v_cvt_pk_bf16_f32 v189, v68, v69
	v_cvt_pk_bf16_f32 v195, v80, v81
	s_waitcnt lgkmcnt(7)
	v_mfma_f32_32x32x16_bf16 v[82:97], v[200:203], v[126:129], v[82:97]
	ds_read_b128 v[196:199], v204
	v_sub_f32_e32 v70, v70, v183
	v_exp_f32_e32 v70, v70
	s_waitcnt lgkmcnt(7)
	v_mfma_f32_32x32x16_bf16 v[82:97], v[216:219], v[122:125], v[82:97]
	ds_read_b128 v[200:203], v204 offset:32
	v_sub_f32_e32 v71, v71, v183
	v_exp_f32_e32 v71, v71
	s_nop 0
	v_cvt_pk_bf16_f32 v190, v70, v71
	s_waitcnt lgkmcnt(7)
	v_mfma_f32_32x32x16_bf16 v[82:97], v[220:223], v[118:121], v[82:97]
	ds_read_b128 v[216:219], v204 offset:4608
	v_sub_f32_e32 v72, v72, v183
	v_exp_f32_e32 v72, v72
	s_waitcnt lgkmcnt(7)
	v_mfma_f32_32x32x16_bf16 v[82:97], v[224:227], v[114:117], v[82:97]
	ds_read_b128 v[220:223], v204 offset:4640
	v_sub_f32_e32 v73, v73, v183
	v_exp_f32_e32 v73, v73
	s_nop 0
	v_cvt_pk_bf16_f32 v191, v72, v73
	s_waitcnt lgkmcnt(7)
	v_mfma_f32_32x32x16_bf16 v[82:97], v[228:231], v[110:113], v[82:97]
	ds_read_b128 v[224:227], v204 offset:9216
	v_sub_f32_e32 v74, v74, v183
	v_exp_f32_e32 v74, v74
	s_waitcnt lgkmcnt(7)
	v_mfma_f32_32x32x16_bf16 v[82:97], v[232:235], v[106:109], v[82:97]
	ds_read_b128 v[228:231], v204 offset:9248
	v_sub_f32_e32 v75, v75, v183
	v_exp_f32_e32 v75, v75
	s_nop 0
	v_cvt_pk_bf16_f32 v192, v74, v75
	s_waitcnt lgkmcnt(7)
	v_mfma_f32_32x32x16_bf16 v[82:97], v[236:239], v[102:105], v[82:97]
	ds_read_b128 v[232:235], v204 offset:13824
	v_sub_f32_e32 v76, v76, v183
	v_exp_f32_e32 v76, v76
	s_waitcnt lgkmcnt(7)
	v_mfma_f32_32x32x16_bf16 v[82:97], v[240:243], v[98:101], v[82:97]
	ds_read_b128 v[236:239], v204 offset:13856
	v_sub_f32_e32 v77, v77, v183
	v_exp_f32_e32 v77, v77
	s_nop 0
	v_cvt_pk_bf16_f32 v193, v76, v77
	s_and_b64 vcc, exec, s[0:1]
	s_cbranch_vccnz .LattA_slow
	s_mul_i32 s12, s36, 0x6400
	s_add_u32 s16, s80, s2
	s_addc_u32 s17, s81, s3
	s_add_u32 s16, s16, 0x30e8a000
	s_addc_u32 s17, s17, 0
	s_waitcnt lgkmcnt(7)
	v_mfma_f32_32x32x16_bf16 v[50:65], v[196:199], v[188:191], v[50:65]
	s_add_i32 m0, s12, s65
	s_nop 0
	global_load_lds_dwordx4 v208, s[16:17]
	s_waitcnt lgkmcnt(5)
	v_mfma_f32_32x32x16_bf16 v[34:49], v[216:219], v[188:191], v[34:49]
	s_add_i32 m0, s12, s66
	s_nop 0
	global_load_lds_dwordx4 v209, s[16:17]
	s_waitcnt lgkmcnt(3)
	v_mfma_f32_32x32x16_bf16 v[18:33], v[224:227], v[188:191], v[18:33]
	v_max_f32_e32 v152, v82, v83
	v_max3_f32 v152, v152, v84, v85
	s_add_i32 m0, s12, s67
	s_add_i32 s12, s12, s68
	global_load_lds_dwordx4 v210, s[16:17]
	s_waitcnt lgkmcnt(1)
	v_mfma_f32_32x32x16_bf16 v[2:17], v[232:235], v[188:191], v[2:17]
	v_max3_f32 v152, v152, v86, v87
	v_max3_f32 v152, v152, v88, v89
	s_add_i32 m0, s12, 0x6000
	s_nop 0
	global_load_lds_dwordx4 v211, s[16:17]
	v_mfma_f32_32x32x16_bf16 v[50:65], v[200:203], v[192:195], v[50:65]
	v_max3_f32 v152, v152, v90, v91
	v_max3_f32 v152, v152, v92, v93
	s_mul_i32 s12, s36, 0x4800
	s_add_i32 s13, s12, 0xffffb800
	s_cmp_lg_u32 s36, 0
	s_cselect_b32 s13, s13, 0x9000
	s_add_i32 s13, s13, 0x12c00
	s_add_u32 s16, s82, s2
	s_addc_u32 s17, s83, s3
	s_add_u32 s16, s16, s28
	s_addc_u32 s17, s17, s29
	s_add_i32 m0, s13, s69
	s_nop 0
	global_load_lds_dwordx4 v212, s[16:17]
	v_mfma_f32_32x32x16_bf16 v[34:49], v[220:223], v[192:195], v[34:49]
	v_max3_f32 v152, v152, v94, v95
	v_max3_f32 v152, v152, v96, v97
	s_add_i32 m0, s13, s70
	s_nop 0
	global_load_lds_dwordx4 v213, s[16:17]
	v_mfma_f32_32x32x16_bf16 v[18:33], v[228:231], v[192:195], v[18:33]
	s_add_i32 m0, s13, s71
	s_nop 0
	global_load_lds_dwordx4 v214, s[16:17]
	s_waitcnt lgkmcnt(0)
	v_mfma_f32_32x32x16_bf16 v[2:17], v[236:239], v[192:195], v[2:17]
	v_mov_b32_e32 v153, v152
	s_nop 1
	v_permlane32_swap_b32_e32 v153, v152
	v_max_f32_e32 v152, v152, v153
	s_branch .LattA_join
